# MoE down GEMM: sibling-shared L2 touch prefetch of the weight tile 3 tiles ahead, issued at the end of each K-tile (behind the last real load) so the in-order vmcnt gives it 1.5 tiles to land
# baseline (speedup 1.0000x reference)
.Lrot_m2:
	ds_read_b64_tr_b16 v[210:211], v234
	ds_read_b64_tr_b16 v[212:213], v234 offset:2048
	ds_read_b64_tr_b16 v[214:215], v238
	ds_read_b64_tr_b16 v[216:217], v238 offset:2048
	ds_read_b128 v[162:165], v235
	ds_read_b128 v[166:169], v235 offset:2048
	ds_read_b64_tr_b16 v[218:219], v240
	ds_read_b64_tr_b16 v[220:221], v240 offset:2048
	ds_read_b64_tr_b16 v[222:223], v242
	ds_read_b64_tr_b16 v[224:225], v242 offset:2048
	s_waitcnt lgkmcnt(5)
	v_mfma_f32_16x16x32_bf16 v[34:37], v[210:213], v[162:165], v[34:37]
	ds_read_b128 v[226:229], v235 offset:4096
	s_and_b32 s42, s37, 0x8000
	v_add_u32_e32 v230, 0xffef8000, v209
	v_mfma_f32_16x16x32_bf16 v[38:41], v[214:217], v[162:165], v[38:41]
	s_add_i32 s43, s36, s39
	s_mov_b32 s44, m0
	s_mov_b32 m0, s43
	s_nop 0
	global_load_lds_dwordx4 v230, s[14:15]
	s_mov_b32 m0, s44
	s_waitcnt lgkmcnt(3)
	v_mfma_f32_16x16x32_bf16 v[42:45], v[218:221], v[162:165], v[42:45]
	s_waitcnt lgkmcnt(1)
	v_mfma_f32_16x16x32_bf16 v[46:49], v[222:225], v[162:165], v[46:49]
	v_mfma_f32_16x16x32_bf16 v[50:53], v[210:213], v[166:169], v[50:53]
	ds_read_b128 v[162:165], v235 offset:6144
	v_add_u32_e32 v230, 0xfff50000, v209
	s_add_i32 s44, s43, 0x2000
	v_mfma_f32_16x16x32_bf16 v[54:57], v[214:217], v[166:169], v[54:57]
	s_mov_b32 s45, m0
	s_mov_b32 m0, s44
	s_nop 0
	global_load_lds_dwordx4 v230, s[14:15]
	s_mov_b32 m0, s45
	v_mfma_f32_16x16x32_bf16 v[58:61], v[218:221], v[166:169], v[58:61]
	v_mfma_f32_16x16x32_bf16 v[62:65], v[222:225], v[166:169], v[62:65]
	s_waitcnt lgkmcnt(1)
	v_mfma_f32_16x16x32_bf16 v[66:69], v[210:213], v[226:229], v[66:69]
	ds_read_b128 v[166:169], v235 offset:8192
	v_add_u32_e32 v230, 0xfffa8000, v209
	s_add_i32 s44, s43, 0x4000
	v_mfma_f32_16x16x32_bf16 v[70:73], v[214:217], v[226:229], v[70:73]
	s_mov_b32 s45, m0
	s_mov_b32 m0, s44
	s_nop 0
	global_load_lds_dwordx4 v230, s[14:15]
	s_mov_b32 m0, s45
	v_mfma_f32_16x16x32_bf16 v[74:77], v[218:221], v[226:229], v[74:77]
	v_mfma_f32_16x16x32_bf16 v[78:81], v[222:225], v[226:229], v[78:81]
	s_waitcnt lgkmcnt(1)
	v_mfma_f32_16x16x32_bf16 v[82:85], v[210:213], v[162:165], v[82:85]
	ds_read_b128 v[226:229], v235 offset:10240
	s_addk_i32 s43, 0x6000
	s_mov_b32 s44, m0
	s_mov_b32 m0, s43
	s_nop 0
	global_load_lds_dwordx4 v209, s[14:15]
	s_mov_b32 m0, s44
	v_mfma_f32_16x16x32_bf16 v[86:89], v[214:217], v[162:165], v[86:89]
	v_mfma_f32_16x16x32_bf16 v[90:93], v[218:221], v[162:165], v[90:93]
	v_mfma_f32_16x16x32_bf16 v[94:97], v[222:225], v[162:165], v[94:97]
	ds_read_b128 v[230:233], v235 offset:12288
	ds_read_b64_tr_b16 v[162:163], v234 offset:16384
	ds_read_b64_tr_b16 v[164:165], v234 offset:18432
	s_waitcnt lgkmcnt(4)
	v_mfma_f32_16x16x32_bf16 v[98:101], v[210:213], v[166:169], v[98:101]
	v_mfma_f32_16x16x32_bf16 v[102:105], v[214:217], v[166:169], v[102:105]
	v_mfma_f32_16x16x32_bf16 v[106:109], v[218:221], v[166:169], v[106:109]
	v_mfma_f32_16x16x32_bf16 v[110:113], v[222:225], v[166:169], v[110:113]
	ds_read_b128 v[234:237], v235 offset:14336
	ds_read_b64_tr_b16 v[166:167], v238 offset:16384
	ds_read_b64_tr_b16 v[168:169], v238 offset:18432
	s_waitcnt lgkmcnt(6)
	v_mfma_f32_16x16x32_bf16 v[114:117], v[210:213], v[226:229], v[114:117]
	v_mfma_f32_16x16x32_bf16 v[118:121], v[214:217], v[226:229], v[118:121]
	v_mfma_f32_16x16x32_bf16 v[122:125], v[218:221], v[226:229], v[122:125]
	v_mfma_f32_16x16x32_bf16 v[126:129], v[222:225], v[226:229], v[126:129]
	v_add_u32_e32 v243, s41, v208
	ds_read_b128 v[226:229], v243
	ds_read_b64_tr_b16 v[238:239], v240 offset:16384
	ds_read_b64_tr_b16 v[240:241], v240 offset:18432
	s_waitcnt lgkmcnt(8)
	v_mfma_f32_16x16x32_bf16 v[130:133], v[210:213], v[230:233], v[130:133]
	v_mfma_f32_16x16x32_bf16 v[134:137], v[214:217], v[230:233], v[134:137]
	v_mfma_f32_16x16x32_bf16 v[138:141], v[218:221], v[230:233], v[138:141]
	v_mfma_f32_16x16x32_bf16 v[142:145], v[222:225], v[230:233], v[142:145]
	s_waitcnt lgkmcnt(5)
	v_mfma_f32_16x16x32_bf16 v[146:149], v[210:213], v[234:237], v[146:149]
	ds_read_b128 v[210:213], v243 offset:2048
	s_add_i32 s41, s24, s42
	v_mfma_f32_16x16x32_bf16 v[150:153], v[214:217], v[234:237], v[150:153]
	ds_read_b64_tr_b16 v[214:215], v242 offset:16384
	ds_read_b64_tr_b16 v[216:217], v242 offset:18432
	v_mfma_f32_16x16x32_bf16 v[158:161], v[218:221], v[234:237], v[158:161]
	v_mfma_f32_16x16x32_bf16 v[154:157], v[222:225], v[234:237], v[154:157]
	ds_read_b128 v[218:221], v243 offset:4096
	s_waitcnt lgkmcnt(6)
	v_mfma_f32_16x16x32_bf16 v[34:37], v[162:165], v[226:229], v[34:37]
	s_add_u32 s44, s2, s16
	s_waitcnt vmcnt(13)
	s_addc_u32 s45, s38, s17
	v_mfma_f32_16x16x32_bf16 v[38:41], v[166:169], v[226:229], v[38:41]
	v_cvt_pk_bf16_f32 v30, v30, v31
	v_cvt_pk_bf16_f32 v31, v32, v33
	v_add_u32_e32 v230, s41, v206
	s_waitcnt lgkmcnt(4)
	v_mfma_f32_16x16x32_bf16 v[42:45], v[238:241], v[226:229], v[42:45]
	s_add_u32 s42, s44, 0x100000
	ds_write_b64 v230, v[30:31]
	s_addc_u32 s43, s45, 0
	s_waitcnt lgkmcnt(2)
	v_mfma_f32_16x16x32_bf16 v[46:49], v[214:217], v[226:229], v[46:49]
	global_load_dwordx4 v[30:33], v199, s[42:43] nt
	v_mfma_f32_16x16x32_bf16 v[50:53], v[162:165], v[210:213], v[50:53]
	ds_read_b128 v[222:225], v243 offset:6144
	s_waitcnt vmcnt(13)
	v_add_u32_e32 v226, s41, v205
	v_mfma_f32_16x16x32_bf16 v[54:57], v[166:169], v[210:213], v[54:57]
	v_cvt_pk_bf16_f32 v26, v26, v27
	v_cvt_pk_bf16_f32 v27, v28, v29
	s_add_u32 s42, s44, 0x110000
	v_mfma_f32_16x16x32_bf16 v[58:61], v[238:241], v[210:213], v[58:61]
	ds_write_b64 v226, v[26:27] offset:4096
	s_addc_u32 s43, s45, 0
	global_load_dwordx4 v[26:29], v199, s[42:43] nt
	v_mfma_f32_16x16x32_bf16 v[62:65], v[214:217], v[210:213], v[62:65]
	s_waitcnt lgkmcnt(3)
	v_mfma_f32_16x16x32_bf16 v[66:69], v[162:165], v[218:221], v[66:69]
	ds_read_b128 v[210:213], v243 offset:8192
	s_waitcnt vmcnt(13)
	s_add_u32 s42, s44, 0x120000
	v_mfma_f32_16x16x32_bf16 v[70:73], v[166:169], v[218:221], v[70:73]
	v_cvt_pk_bf16_f32 v22, v22, v23
	v_cvt_pk_bf16_f32 v23, v24, v25
	ds_write_b64 v230, v[22:23] offset:8192
	v_mfma_f32_16x16x32_bf16 v[74:77], v[238:241], v[218:221], v[74:77]
	s_addc_u32 s43, s45, 0
	global_load_dwordx4 v[22:25], v199, s[42:43] nt
	v_mfma_f32_16x16x32_bf16 v[78:81], v[214:217], v[218:221], v[78:81]
	s_waitcnt lgkmcnt(3)
	v_mfma_f32_16x16x32_bf16 v[82:85], v[162:165], v[222:225], v[82:85]
	ds_read_b128 v[218:221], v243 offset:10240
	s_waitcnt vmcnt(13)
	s_add_u32 s42, s44, 0x130000
	v_mfma_f32_16x16x32_bf16 v[86:89], v[166:169], v[222:225], v[86:89]
	v_cvt_pk_bf16_f32 v18, v18, v19
	v_cvt_pk_bf16_f32 v19, v20, v21
	ds_write_b64 v226, v[18:19] offset:12288
	v_mfma_f32_16x16x32_bf16 v[90:93], v[238:241], v[222:225], v[90:93]
	s_addc_u32 s43, s45, 0
	global_load_dwordx4 v[18:21], v199, s[42:43] nt
	v_mfma_f32_16x16x32_bf16 v[94:97], v[214:217], v[222:225], v[94:97]
	s_waitcnt lgkmcnt(3)
	v_mfma_f32_16x16x32_bf16 v[98:101], v[162:165], v[210:213], v[98:101]
	ds_read_b128 v[222:225], v243 offset:12288
	s_waitcnt vmcnt(13)
	s_add_u32 s42, s44, 0x140000
	v_mfma_f32_16x16x32_bf16 v[102:105], v[166:169], v[210:213], v[102:105]
	v_cvt_pk_bf16_f32 v14, v14, v15
	v_cvt_pk_bf16_f32 v15, v16, v17
	ds_write_b64 v230, v[14:15] offset:16384
	v_mfma_f32_16x16x32_bf16 v[106:109], v[238:241], v[210:213], v[106:109]
	s_addc_u32 s43, s45, 0
	global_load_dwordx4 v[14:17], v199, s[42:43] nt
	v_mfma_f32_16x16x32_bf16 v[110:113], v[214:217], v[210:213], v[110:113]
	s_waitcnt lgkmcnt(3)
	v_mfma_f32_16x16x32_bf16 v[114:117], v[162:165], v[218:221], v[114:117]
	ds_read_b128 v[210:213], v243 offset:14336
	s_waitcnt vmcnt(13)
	s_add_u32 s42, s44, 0x150000
	v_mfma_f32_16x16x32_bf16 v[118:121], v[166:169], v[218:221], v[118:121]
	v_cvt_pk_bf16_f32 v10, v10, v11
	v_cvt_pk_bf16_f32 v11, v12, v13
	ds_write_b64 v226, v[10:11] offset:20480
	v_mfma_f32_16x16x32_bf16 v[122:125], v[238:241], v[218:221], v[122:125]
	s_addc_u32 s43, s45, 0
	global_load_dwordx4 v[10:13], v199, s[42:43] nt
	v_mfma_f32_16x16x32_bf16 v[126:129], v[214:217], v[218:221], v[126:129]
	s_waitcnt lgkmcnt(3)
	v_mfma_f32_16x16x32_bf16 v[130:133], v[162:165], v[222:225], v[130:133]
	s_waitcnt vmcnt(13)
	s_add_u32 s42, s44, 0x160000
	v_cvt_pk_bf16_f32 v6, v6, v7
	v_mfma_f32_16x16x32_bf16 v[134:137], v[166:169], v[222:225], v[134:137]
	v_cvt_pk_bf16_f32 v7, v8, v9
	ds_write_b64 v230, v[6:7] offset:24576
	s_addc_u32 s43, s45, 0
	v_mfma_f32_16x16x32_bf16 v[138:141], v[238:241], v[222:225], v[138:141]
	global_load_dwordx4 v[6:9], v199, s[42:43] nt
	v_mfma_f32_16x16x32_bf16 v[142:145], v[214:217], v[222:225], v[142:145]
	s_waitcnt lgkmcnt(2)
	v_mfma_f32_16x16x32_bf16 v[146:149], v[162:165], v[210:213], v[146:149]
	s_waitcnt vmcnt(13)
	s_add_u32 s42, s44, 0x170000
	v_cvt_pk_bf16_f32 v2, v2, v3
	v_mfma_f32_16x16x32_bf16 v[150:153], v[166:169], v[210:213], v[150:153]
	v_cvt_pk_bf16_f32 v3, v4, v5
	ds_write_b64 v226, v[2:3] offset:28672
	s_addc_u32 s43, s45, 0
	v_mfma_f32_16x16x32_bf16 v[158:161], v[238:241], v[210:213], v[158:161]
	global_load_dwordx4 v[2:5], v199, s[42:43] nt
	v_mfma_f32_16x16x32_bf16 v[154:157], v[214:217], v[210:213], v[154:157]
	s_add_u32 s94, s16, 0x180000
	s_min_u32 s94, s94, 0x1580000
	s_and_b32 s95, s29, 3
	s_lshl_b32 s95, s95, 17
	s_add_u32 s94, s94, s95
	s_add_u32 s94, s2, s94
	s_addc_u32 s95, s38, 0
	global_load_dword v245, v199, s[94:95]
	s_add_u32 s94, s94, 0x10000
	s_addc_u32 s95, s95, 0
	global_load_dword v245, v199, s[94:95]
	s_add_i32 s41, s40, 0x8000
	s_cmp_lg_u32 s40, 0x10000
	s_cselect_b32 s40, s41, 0
	s_add_i32 s41, s39, 0x8000
	s_cmp_lg_u32 s39, 0x10000
	s_cselect_b32 s39, s41, 0
	s_add_u32 s16, s16, 0x80000
	s_addc_u32 s17, s17, 0
	s_add_i32 s37, s37, 0x8000
	v_add_u32_e32 v209, 0x80, v209
	s_add_i32 s42, s37, 0xffff8000
	s_and_b32 s42, s42, 0x8000
	s_add_i32 s41, s40, 0
	s_add_i32 s42, s24, s42
	v_add_u32_e32 v234, s42, v183
	v_add_u32_e32 v235, s41, v207
	v_add_u32_e32 v240, s42, v179
	v_add_u32_e32 v242, s42, v172
	v_add_u32_e32 v238, s42, v181
	s_waitcnt lgkmcnt(0)
	s_barrier
	s_cmp_lg_u32 s16, 0x1500000
	s_cbranch_scc1 .Lrot_m2
	v_add_u32_e32 v209, s24, v183
	v_add_u32_e32 v242, 0, v207
	v_add_u32_e32 v207, s24, v179
	v_add_u32_e32 v243, s24, v172
	v_add_u32_e32 v236, s24, v181
	ds_read_b64_tr_b16 v[162:163], v209
	ds_read_b64_tr_b16 v[164:165], v209 offset:2048
	ds_read_b64_tr_b16 v[166:167], v236
	ds_read_b64_tr_b16 v[168:169], v236 offset:2048
	ds_read_b128 v[210:213], v242
	ds_read_b128 v[214:217], v242 offset:2048
	ds_read_b64_tr_b16 v[218:219], v207
	ds_read_b64_tr_b16 v[220:221], v207 offset:2048
	ds_read_b64_tr_b16 v[222:223], v243
	ds_read_b64_tr_b16 v[224:225], v243 offset:2048
	s_waitcnt lgkmcnt(5)
	v_mfma_f32_16x16x32_bf16 v[34:37], v[162:165], v[210:213], v[34:37]
	ds_read_b128 v[226:229], v242 offset:4096
	v_mfma_f32_16x16x32_bf16 v[38:41], v[166:169], v[210:213], v[38:41]
	s_waitcnt lgkmcnt(3)
	v_mfma_f32_16x16x32_bf16 v[42:45], v[218:221], v[210:213], v[42:45]
	s_waitcnt lgkmcnt(1)
	v_mfma_f32_16x16x32_bf16 v[46:49], v[222:225], v[210:213], v[46:49]
	v_mfma_f32_16x16x32_bf16 v[50:53], v[162:165], v[214:217], v[50:53]
	ds_read_b128 v[210:213], v242 offset:6144
	v_mfma_f32_16x16x32_bf16 v[54:57], v[166:169], v[214:217], v[54:57]
	v_mfma_f32_16x16x32_bf16 v[58:61], v[218:221], v[214:217], v[58:61]
	v_mfma_f32_16x16x32_bf16 v[62:65], v[222:225], v[214:217], v[62:65]
	s_waitcnt lgkmcnt(1)
	v_mfma_f32_16x16x32_bf16 v[66:69], v[162:165], v[226:229], v[66:69]
	ds_read_b128 v[214:217], v242 offset:8192
	v_mfma_f32_16x16x32_bf16 v[70:73], v[166:169], v[226:229], v[70:73]
	v_mfma_f32_16x16x32_bf16 v[74:77], v[218:221], v[226:229], v[74:77]
	v_mfma_f32_16x16x32_bf16 v[78:81], v[222:225], v[226:229], v[78:81]
	s_waitcnt lgkmcnt(1)
	v_mfma_f32_16x16x32_bf16 v[82:85], v[162:165], v[210:213], v[82:85]
	ds_read_b128 v[226:229], v242 offset:10240
	v_mfma_f32_16x16x32_bf16 v[86:89], v[166:169], v[210:213], v[86:89]
	v_mfma_f32_16x16x32_bf16 v[90:93], v[218:221], v[210:213], v[90:93]
	v_mfma_f32_16x16x32_bf16 v[94:97], v[222:225], v[210:213], v[94:97]
	ds_read_b128 v[210:213], v242 offset:12288
	ds_read_b64_tr_b16 v[230:231], v209 offset:16384
	ds_read_b64_tr_b16 v[232:233], v209 offset:18432
	s_waitcnt lgkmcnt(4)
	v_mfma_f32_16x16x32_bf16 v[98:101], v[162:165], v[214:217], v[98:101]
	v_mfma_f32_16x16x32_bf16 v[102:105], v[166:169], v[214:217], v[102:105]
	v_mfma_f32_16x16x32_bf16 v[106:109], v[218:221], v[214:217], v[106:109]
	v_mfma_f32_16x16x32_bf16 v[110:113], v[222:225], v[214:217], v[110:113]
	ds_read_b128 v[214:217], v242 offset:14336
	ds_read_b64_tr_b16 v[234:235], v236 offset:16384
	ds_read_b64_tr_b16 v[236:237], v236 offset:18432
	s_waitcnt lgkmcnt(6)
	v_mfma_f32_16x16x32_bf16 v[114:117], v[162:165], v[226:229], v[114:117]
	v_mfma_f32_16x16x32_bf16 v[118:121], v[166:169], v[226:229], v[118:121]
	v_mfma_f32_16x16x32_bf16 v[122:125], v[218:221], v[226:229], v[122:125]
	v_mfma_f32_16x16x32_bf16 v[126:129], v[222:225], v[226:229], v[126:129]
	v_add_u32_e32 v244, 0, v208
	ds_read_b128 v[226:229], v244
	ds_read_b64_tr_b16 v[238:239], v207 offset:16384
	ds_read_b64_tr_b16 v[240:241], v207 offset:18432
	s_waitcnt lgkmcnt(8)
	v_mfma_f32_16x16x32_bf16 v[130:133], v[162:165], v[210:213], v[130:133]
	v_mfma_f32_16x16x32_bf16 v[134:137], v[166:169], v[210:213], v[134:137]
	v_mfma_f32_16x16x32_bf16 v[138:141], v[218:221], v[210:213], v[138:141]
	v_mfma_f32_16x16x32_bf16 v[142:145], v[222:225], v[210:213], v[142:145]
	s_waitcnt lgkmcnt(5)
	v_mfma_f32_16x16x32_bf16 v[146:149], v[162:165], v[214:217], v[146:149]
	v_mfma_f32_16x16x32_bf16 v[150:153], v[166:169], v[214:217], v[150:153]
	ds_read_b128 v[162:165], v244 offset:2048
	ds_read_b64_tr_b16 v[166:167], v243 offset:16384
	ds_read_b64_tr_b16 v[168:169], v243 offset:18432
	v_mfma_f32_16x16x32_bf16 v[158:161], v[218:221], v[214:217], v[158:161]
	v_mfma_f32_16x16x32_bf16 v[154:157], v[222:225], v[214:217], v[154:157]
	ds_read_b128 v[208:211], v244 offset:4096
	s_waitcnt vmcnt(7)
	v_add_u32_e32 v206, s25, v206
	v_cvt_pk_bf16_f32 v30, v30, v31
	v_cvt_pk_bf16_f32 v31, v32, v33
	s_waitcnt lgkmcnt(6)
	v_mfma_f32_16x16x32_bf16 v[34:37], v[230:233], v[226:229], v[34:37]
	ds_write_b64 v206, v[30:31]
	v_mfma_f32_16x16x32_bf16 v[38:41], v[234:237], v[226:229], v[38:41]
	s_waitcnt lgkmcnt(5)
	v_mfma_f32_16x16x32_bf16 v[42:45], v[238:241], v[226:229], v[42:45]
	s_waitcnt lgkmcnt(2)
	v_mfma_f32_16x16x32_bf16 v[30:33], v[166:169], v[226:229], v[46:49]
	v_mfma_f32_16x16x32_bf16 v[46:49], v[230:233], v[162:165], v[50:53]
	v_add_u32_e32 v205, s25, v205
	v_mfma_f32_16x16x32_bf16 v[50:53], v[234:237], v[162:165], v[54:57]
	s_nop 2
	ds_read_b128 v[54:57], v244 offset:6144
	s_waitcnt vmcnt(6)
	v_mfma_f32_16x16x32_bf16 v[58:61], v[238:241], v[162:165], v[58:61]
	v_cvt_pk_bf16_f32 v26, v26, v27
	v_cvt_pk_bf16_f32 v27, v28, v29
	ds_write_b64 v205, v[26:27] offset:4096
	v_mfma_f32_16x16x32_bf16 v[26:29], v[166:169], v[162:165], v[62:65]
	s_waitcnt lgkmcnt(3)
	v_mfma_f32_16x16x32_bf16 v[62:65], v[230:233], v[208:211], v[66:69]
	v_mfma_f32_16x16x32_bf16 v[66:69], v[234:237], v[208:211], v[70:73]
	s_nop 2
	ds_read_b128 v[70:73], v244 offset:8192
	s_waitcnt vmcnt(5)
	v_mfma_f32_16x16x32_bf16 v[74:77], v[238:241], v[208:211], v[74:77]
	v_cvt_pk_bf16_f32 v22, v22, v23
	v_cvt_pk_bf16_f32 v23, v24, v25
	ds_write_b64 v206, v[22:23] offset:8192
	v_mfma_f32_16x16x32_bf16 v[22:25], v[166:169], v[208:211], v[78:81]
	s_waitcnt lgkmcnt(3)
	v_mfma_f32_16x16x32_bf16 v[78:81], v[230:233], v[54:57], v[82:85]
	v_mfma_f32_16x16x32_bf16 v[82:85], v[234:237], v[54:57], v[86:89]
	s_nop 2
	ds_read_b128 v[86:89], v244 offset:10240
	s_waitcnt vmcnt(4)
	v_mfma_f32_16x16x32_bf16 v[90:93], v[238:241], v[54:57], v[90:93]
	v_cvt_pk_bf16_f32 v18, v18, v19
	v_cvt_pk_bf16_f32 v19, v20, v21
	ds_write_b64 v205, v[18:19] offset:12288
	v_mfma_f32_16x16x32_bf16 v[18:21], v[166:169], v[54:57], v[94:97]
	s_waitcnt lgkmcnt(3)
	v_mfma_f32_16x16x32_bf16 v[54:57], v[230:233], v[70:73], v[98:101]
	s_nop 2
	ds_read_b128 v[98:101], v244 offset:12288
	s_waitcnt vmcnt(3)
	v_mfma_f32_16x16x32_bf16 v[94:97], v[234:237], v[70:73], v[102:105]
	v_cvt_pk_bf16_f32 v14, v14, v15
	v_cvt_pk_bf16_f32 v15, v16, v17
	ds_write_b64 v206, v[14:15] offset:16384
	v_mfma_f32_16x16x32_bf16 v[102:105], v[238:241], v[70:73], v[106:109]
	v_mfma_f32_16x16x32_bf16 v[14:17], v[166:169], v[70:73], v[110:113]
	s_nop 2
	ds_read_b128 v[110:113], v244 offset:14336
	s_waitcnt vmcnt(2)
	s_waitcnt lgkmcnt(4)
	v_mfma_f32_16x16x32_bf16 v[70:73], v[230:233], v[86:89], v[114:117]
	v_cvt_pk_bf16_f32 v10, v10, v11
	v_cvt_pk_bf16_f32 v11, v12, v13
	ds_write_b64 v205, v[10:11] offset:20480
	v_mfma_f32_16x16x32_bf16 v[106:109], v[234:237], v[86:89], v[118:121]
	v_mfma_f32_16x16x32_bf16 v[114:117], v[238:241], v[86:89], v[122:125]
	v_mfma_f32_16x16x32_bf16 v[10:13], v[166:169], v[86:89], v[126:129]
	s_waitcnt vmcnt(1)
	s_waitcnt lgkmcnt(3)
	v_mfma_f32_16x16x32_bf16 v[86:89], v[230:233], v[98:101], v[130:133]
	v_cvt_pk_bf16_f32 v6, v6, v7
	v_cvt_pk_bf16_f32 v7, v8, v9
	ds_write_b64 v206, v[6:7] offset:24576
	v_mfma_f32_16x16x32_bf16 v[118:121], v[234:237], v[98:101], v[134:137]
	v_mfma_f32_16x16x32_bf16 v[122:125], v[238:241], v[98:101], v[138:141]
	v_mfma_f32_16x16x32_bf16 v[6:9], v[166:169], v[98:101], v[142:145]
	s_waitcnt vmcnt(0)
	s_waitcnt lgkmcnt(2)
	v_mfma_f32_16x16x32_bf16 v[98:101], v[230:233], v[110:113], v[146:149]
	v_cvt_pk_bf16_f32 v2, v2, v3
	v_cvt_pk_bf16_f32 v3, v4, v5
	ds_write_b64 v205, v[2:3] offset:28672
	v_mfma_f32_16x16x32_bf16 v[126:129], v[234:237], v[110:113], v[150:153]
	v_mfma_f32_16x16x32_bf16 v[130:133], v[238:241], v[110:113], v[158:161]
	v_mfma_f32_16x16x32_bf16 v[2:5], v[166:169], v[110:113], v[154:157]
	s_waitcnt lgkmcnt(0)
	s_barrier
	v_add_u32_e32 v168, s25, v183
	v_add_u32_e32 v181, s25, v181
	v_add_u32_e32 v179, s25, v179
	ds_read_b64_tr_b16 v[110:111], v168
	ds_read_b64_tr_b16 v[112:113], v168 offset:2048
	ds_read_b64_tr_b16 v[134:135], v181
	ds_read_b64_tr_b16 v[136:137], v181 offset:2048
	ds_read_b128 v[138:141], v242 offset:32768
	ds_read_b64_tr_b16 v[142:143], v179
	ds_read_b128 v[146:149], v242 offset:34816
	ds_read_b128 v[150:153], v242 offset:36864
	ds_read_b64_tr_b16 v[144:145], v179 offset:2048
	v_add_u32_e32 v172, s25, v172
	ds_read_b64_tr_b16 v[154:155], v172
	ds_read_b64_tr_b16 v[156:157], v172 offset:2048
	s_waitcnt lgkmcnt(6)
	v_mfma_f32_16x16x32_bf16 v[34:37], v[110:113], v[138:141], v[34:37]
	v_mfma_f32_16x16x32_bf16 v[38:41], v[134:137], v[138:141], v[38:41]
	s_waitcnt lgkmcnt(2)
	v_mfma_f32_16x16x32_bf16 v[42:45], v[142:145], v[138:141], v[42:45]
	s_waitcnt lgkmcnt(0)
	v_mfma_f32_16x16x32_bf16 v[30:33], v[154:157], v[138:141], v[30:33]
	v_mfma_f32_16x16x32_bf16 v[46:49], v[110:113], v[146:149], v[46:49]
	ds_read_b128 v[138:141], v242 offset:38912
	v_mfma_f32_16x16x32_bf16 v[50:53], v[134:137], v[146:149], v[50:53]
	v_mfma_f32_16x16x32_bf16 v[58:61], v[142:145], v[146:149], v[58:61]
	v_mfma_f32_16x16x32_bf16 v[26:29], v[154:157], v[146:149], v[26:29]
	v_mfma_f32_16x16x32_bf16 v[62:65], v[110:113], v[150:153], v[62:65]
	ds_read_b128 v[146:149], v242 offset:40960
	v_mfma_f32_16x16x32_bf16 v[66:69], v[134:137], v[150:153], v[66:69]
	v_mfma_f32_16x16x32_bf16 v[74:77], v[142:145], v[150:153], v[74:77]
	v_mfma_f32_16x16x32_bf16 v[22:25], v[154:157], v[150:153], v[22:25]
	s_waitcnt lgkmcnt(1)
	v_mfma_f32_16x16x32_bf16 v[150:153], v[134:137], v[138:141], v[82:85]
	s_nop 2
	ds_read_b128 v[82:85], v242 offset:43008
	v_mfma_f32_16x16x32_bf16 v[78:81], v[110:113], v[138:141], v[78:81]
	v_mfma_f32_16x16x32_bf16 v[18:21], v[154:157], v[138:141], v[18:21]
	v_mfma_f32_16x16x32_bf16 v[158:161], v[142:145], v[138:141], v[90:93]
	s_nop 2
	ds_read_b128 v[90:93], v242 offset:45056
	ds_read_b64_tr_b16 v[166:167], v168 offset:16384
	ds_read_b64_tr_b16 v[168:169], v168 offset:18432
	s_waitcnt lgkmcnt(4)
	v_mfma_f32_16x16x32_bf16 v[54:57], v[110:113], v[146:149], v[54:57]
	v_mfma_f32_16x16x32_bf16 v[14:17], v[154:157], v[146:149], v[14:17]
	v_mfma_f32_16x16x32_bf16 v[138:141], v[134:137], v[146:149], v[94:97]
	v_mfma_f32_16x16x32_bf16 v[162:165], v[142:145], v[146:149], v[102:105]
	s_waitcnt lgkmcnt(3)
	v_mfma_f32_16x16x32_bf16 v[146:149], v[110:113], v[82:85], v[70:73]
	s_nop 2
	ds_read_b128 v[70:73], v242 offset:47104
	ds_read_b64_tr_b16 v[214:215], v181 offset:16384
	ds_read_b64_tr_b16 v[216:217], v181 offset:18432
	v_mfma_f32_16x16x32_bf16 v[10:13], v[154:157], v[82:85], v[10:13]
	v_mfma_f32_16x16x32_bf16 v[206:209], v[134:137], v[82:85], v[106:109]
	v_mfma_f32_16x16x32_bf16 v[210:213], v[142:145], v[82:85], v[114:117]
	ds_read_b128 v[82:85], v244 offset:32768
	ds_read_b64_tr_b16 v[230:231], v179 offset:16384
	ds_read_b64_tr_b16 v[232:233], v179 offset:18432
	s_waitcnt lgkmcnt(8)
	v_mfma_f32_16x16x32_bf16 v[6:9], v[154:157], v[90:93], v[6:9]
	v_mfma_f32_16x16x32_bf16 v[218:221], v[110:113], v[90:93], v[86:89]
	v_mfma_f32_16x16x32_bf16 v[222:225], v[134:137], v[90:93], v[118:121]
	v_mfma_f32_16x16x32_bf16 v[226:229], v[142:145], v[90:93], v[122:125]
	s_waitcnt lgkmcnt(5)
	v_mfma_f32_16x16x32_bf16 v[130:133], v[142:145], v[70:73], v[130:133]
	ds_read_b128 v[86:89], v244 offset:34816
	ds_read_b64_tr_b16 v[142:143], v172 offset:16384
	ds_read_b64_tr_b16 v[144:145], v172 offset:18432
	v_mfma_f32_16x16x32_bf16 v[134:137], v[134:137], v[70:73], v[126:129]
	v_mfma_f32_16x16x32_bf16 v[2:5], v[154:157], v[70:73], v[2:5]
	v_mfma_f32_16x16x32_bf16 v[234:237], v[110:113], v[70:73], v[98:101]
	s_waitcnt lgkmcnt(5)
	v_mfma_f32_16x16x32_bf16 v[126:129], v[166:169], v[82:85], v[34:37]
	s_nop 2
	ds_read_b128 v[34:37], v244 offset:36864
	v_mfma_f32_16x16x32_bf16 v[122:125], v[214:217], v[82:85], v[38:41]
	s_waitcnt lgkmcnt(4)
	v_mfma_f32_16x16x32_bf16 v[118:121], v[230:233], v[82:85], v[42:45]
	s_waitcnt lgkmcnt(1)
	v_mfma_f32_16x16x32_bf16 v[114:117], v[142:145], v[82:85], v[30:33]
	s_nop 2
	ds_read_b128 v[30:33], v244 offset:38912
	v_mfma_f32_16x16x32_bf16 v[110:113], v[166:169], v[86:89], v[46:49]
	v_mfma_f32_16x16x32_bf16 v[106:109], v[214:217], v[86:89], v[50:53]
	v_mfma_f32_16x16x32_bf16 v[102:105], v[230:233], v[86:89], v[58:61]
	v_mfma_f32_16x16x32_bf16 v[98:101], v[142:145], v[86:89], v[26:29]
	s_nop 2
	ds_read_b128 v[26:29], v244 offset:40960
	s_waitcnt lgkmcnt(2)
	v_mfma_f32_16x16x32_bf16 v[94:97], v[166:169], v[34:37], v[62:65]
	v_mfma_f32_16x16x32_bf16 v[90:93], v[214:217], v[34:37], v[66:69]
	v_mfma_f32_16x16x32_bf16 v[86:89], v[230:233], v[34:37], v[74:77]
	v_mfma_f32_16x16x32_bf16 v[82:85], v[142:145], v[34:37], v[22:25]
	s_nop 2
	ds_read_b128 v[22:25], v244 offset:43008
	s_waitcnt lgkmcnt(2)
	v_mfma_f32_16x16x32_bf16 v[78:81], v[166:169], v[30:33], v[78:81]
	v_mfma_f32_16x16x32_bf16 v[74:77], v[214:217], v[30:33], v[150:153]
	v_mfma_f32_16x16x32_bf16 v[70:73], v[230:233], v[30:33], v[158:161]
	v_mfma_f32_16x16x32_bf16 v[66:69], v[142:145], v[30:33], v[18:21]
	s_nop 2
	ds_read_b128 v[18:21], v244 offset:45056
	s_waitcnt lgkmcnt(2)
	v_mfma_f32_16x16x32_bf16 v[62:65], v[166:169], v[26:29], v[54:57]
	v_mfma_f32_16x16x32_bf16 v[58:61], v[214:217], v[26:29], v[138:141]
	v_mfma_f32_16x16x32_bf16 v[54:57], v[230:233], v[26:29], v[162:165]
	v_mfma_f32_16x16x32_bf16 v[50:53], v[142:145], v[26:29], v[14:17]
	s_waitcnt lgkmcnt(1)
	v_mfma_f32_16x16x32_bf16 v[46:49], v[166:169], v[22:25], v[146:149]
	ds_read_b128 v[138:141], v244 offset:47104
	v_mfma_f32_16x16x32_bf16 v[42:45], v[214:217], v[22:25], v[206:209]
	v_mfma_f32_16x16x32_bf16 v[38:41], v[230:233], v[22:25], v[210:213]
	v_mfma_f32_16x16x32_bf16 v[34:37], v[142:145], v[22:25], v[10:13]
	s_waitcnt lgkmcnt(1)
	v_mfma_f32_16x16x32_bf16 v[30:33], v[166:169], v[18:21], v[218:221]
	v_mfma_f32_16x16x32_bf16 v[26:29], v[214:217], v[18:21], v[222:225]
	v_mfma_f32_16x16x32_bf16 v[22:25], v[230:233], v[18:21], v[226:229]
	v_mfma_f32_16x16x32_bf16 v[18:21], v[142:145], v[18:21], v[6:9]
	s_waitcnt lgkmcnt(0)
	v_mfma_f32_16x16x32_bf16 v[14:17], v[166:169], v[138:141], v[234:237]
	v_mfma_f32_16x16x32_bf16 v[10:13], v[214:217], v[138:141], v[134:137]
	v_mfma_f32_16x16x32_bf16 v[6:9], v[230:233], v[138:141], v[130:133]
	v_mfma_f32_16x16x32_bf16 v[2:5], v[142:145], v[138:141], v[2:5]
	s_waitcnt lgkmcnt(0)
	s_barrier
	s_nop 0
	v_mov_b32_e32 v131, 0
	s_andn2_b64 vcc, exec, s[12:13]
	v_mov_b32_e32 v133, 0
	v_mov_b32_e32 v134, 0
	s_cbranch_vccnz .LBB0_1536
	global_load_dword v131, v[184:185], off
	global_load_dword v133, v[186:187], off
	global_load_dword v134, v[188:189], off
	s_branch .LBB0_1536
